# GQA QK^T: K-slice LDS reads double-buffered (second register pair), reads of slice k+1 issued before the MFMAs of slice k, waits re-counted (2 in-loop sections), on top of v63
# speedup vs baseline: 1.0113x; 1.0113x over previous
.LBB0_846:
	ds_read_b128 v[64:67], v177 offset:49152
	ds_read_b128 v[68:71], v177 offset:57344
	ds_read_b128 v[188:191], v178 offset:49152
	ds_read_b128 v[204:207], v178 offset:57344
	ds_read_b128 v[230:233], v179 offset:49152
	ds_read_b128 v[234:237], v179 offset:57344
	v_add_f32_e32 v187, 0, v202
	v_add_f32_e32 v187, v221, v187
	s_waitcnt lgkmcnt(5)
	v_mfma_f32_32x32x16_bf16 v[80:95], v[64:67], v[126:129], 0
	v_add_f32_e32 v187, v222, v187
	v_add_f32_e32 v187, v223, v187
	v_add_f32_e32 v187, v224, v187
	v_add_f32_e32 v187, v225, v187
	v_add_f32_e32 v187, v201, v187
	v_add_f32_e32 v187, v203, v187
	v_add_f32_e32 v187, v196, v187
	s_waitcnt lgkmcnt(4)
	v_mfma_f32_32x32x16_bf16 v[64:79], v[68:71], v[126:129], 0
	v_add_f32_e32 v187, v198, v187
	v_add_f32_e32 v187, v199, v187
	v_add_f32_e32 v187, v200, v187
	v_exp_f32_e32 v142, v142
	v_add_f32_e32 v187, v193, v187
	v_exp_f32_e32 v143, v143
	v_add_f32_e32 v187, v194, v187
	s_waitcnt lgkmcnt(3)
	v_mfma_f32_32x32x16_bf16 v[80:95], v[188:191], v[122:125], v[80:95]
	v_exp_f32_e32 v140, v140
	v_add_f32_e32 v187, v195, v187
	v_exp_f32_e32 v141, v141
	v_add_f32_e32 v187, v197, v187
	v_exp_f32_e32 v134, v134
	v_add_f32_e32 v187, v142, v187
	v_exp_f32_e32 v135, v135
	s_waitcnt lgkmcnt(2)
	v_mfma_f32_32x32x16_bf16 v[64:79], v[204:207], v[122:125], v[64:79]
	ds_read_b128 v[188:191], v180 offset:49152
	ds_read_b128 v[204:207], v180 offset:57344
	v_add_f32_e32 v187, v143, v187
	v_exp_f32_e32 v132, v132
	v_add_f32_e32 v187, v140, v187
	v_exp_f32_e32 v133, v133
	v_add_f32_e32 v187, v141, v187
	v_exp_f32_e32 v130, v130
	s_waitcnt lgkmcnt(3)
	v_mfma_f32_32x32x16_bf16 v[80:95], v[230:233], v[118:121], v[80:95]
	v_add_f32_e32 v187, v134, v187
	v_exp_f32_e32 v131, v131
	v_add_f32_e32 v187, v135, v187
	v_exp_f32_e32 v144, v144
	v_add_f32_e32 v187, v132, v187
	v_exp_f32_e32 v145, v145
	v_add_f32_e32 v187, v133, v187
	s_waitcnt lgkmcnt(2)
	v_mfma_f32_32x32x16_bf16 v[64:79], v[234:237], v[118:121], v[64:79]
	ds_read_b128 v[230:233], v181 offset:49152
	ds_read_b128 v[234:237], v181 offset:57344
	v_exp_f32_e32 v138, v138
	v_add_f32_e32 v187, v130, v187
	v_exp_f32_e32 v139, v139
	v_add_f32_e32 v187, v131, v187
	v_exp_f32_e32 v136, v136
	v_add_f32_e32 v187, v144, v187
	s_waitcnt lgkmcnt(3)
	v_mfma_f32_32x32x16_bf16 v[80:95], v[188:191], v[114:117], v[80:95]
	v_exp_f32_e32 v137, v137
	v_add_f32_e32 v187, v145, v187
	v_add_f32_e32 v187, v138, v187
	v_add_f32_e32 v187, v139, v187
	v_add_f32_e32 v187, v136, v187
	v_add_f32_e32 v187, v137, v187
	v_cvt_pk_bf16_f32 v192, v193, v194
	s_waitcnt lgkmcnt(2)
	v_mfma_f32_32x32x16_bf16 v[64:79], v[204:207], v[114:117], v[64:79]
	ds_read_b128 v[188:191], v182 offset:49152
	ds_read_b128 v[204:207], v182 offset:57344
	v_cvt_pk_bf16_f32 v193, v195, v197
	v_cvt_pk_bf16_f32 v194, v142, v143
	v_cvt_pk_bf16_f32 v195, v140, v141
	v_cvt_pk_bf16_f32 v197, v132, v133
	s_nop 1
	v_permlane32_swap_b32_e32 v195, v197
	s_waitcnt lgkmcnt(3)
	v_mfma_f32_32x32x16_bf16 v[80:95], v[230:233], v[110:113], v[80:95]
	s_waitcnt lgkmcnt(2)
	v_mfma_f32_32x32x16_bf16 v[64:79], v[234:237], v[110:113], v[64:79]
	ds_read_b128 v[230:233], v183 offset:49152
	ds_read_b128 v[234:237], v183 offset:57344
	s_waitcnt lgkmcnt(3)
	v_mfma_f32_32x32x16_bf16 v[80:95], v[188:191], v[106:109], v[80:95]
	s_waitcnt lgkmcnt(2)
	v_mfma_f32_32x32x16_bf16 v[64:79], v[204:207], v[106:109], v[64:79]
	ds_read_b128 v[188:191], v184 offset:49152
	ds_read_b128 v[204:207], v184 offset:57344
	s_waitcnt lgkmcnt(3)
	v_mfma_f32_32x32x16_bf16 v[80:95], v[230:233], v[102:105], v[80:95]
	s_waitcnt lgkmcnt(2)
	v_mfma_f32_32x32x16_bf16 v[64:79], v[234:237], v[102:105], v[64:79]
	s_waitcnt lgkmcnt(1)
	v_mfma_f32_32x32x16_bf16 v[80:95], v[188:191], v[98:101], v[80:95]
	v_mov_b32_e32 v188, v187
	v_cvt_pk_bf16_f32 v190, v196, v198
	s_nop 0
	v_permlane32_swap_b32_e32 v187, v188
	v_cvt_pk_bf16_f32 v191, v199, v200
	v_permlane32_swap_b32_e32 v190, v192
	s_waitcnt lgkmcnt(0)
	v_mfma_f32_32x32x16_bf16 v[64:79], v[204:207], v[98:101], v[64:79]
	v_cvt_pk_bf16_f32 v204, v202, v221
	v_cvt_pk_bf16_f32 v205, v222, v223
	v_cvt_pk_bf16_f32 v206, v224, v225
	v_cvt_pk_bf16_f32 v207, v201, v203
	v_cvt_pk_bf16_f32 v196, v134, v135
	v_cvt_pk_bf16_f32 v198, v130, v131
	v_cvt_pk_bf16_f32 v199, v144, v145
	v_cvt_pk_bf16_f32 v200, v138, v139
	v_cvt_pk_bf16_f32 v201, v136, v137
	v_permlane32_swap_b32_e32 v204, v206
	v_permlane32_swap_b32_e32 v205, v207
	v_permlane32_swap_b32_e32 v191, v193
	v_permlane32_swap_b32_e32 v194, v196
	v_permlane32_swap_b32_e32 v198, v200
	v_permlane32_swap_b32_e32 v199, v201
	v_add_co_u32_e32 v138, vcc, s65, v166
	s_nop 1
	v_addc_co_u32_e32 v139, vcc, 0, v167, vcc
	global_load_dwordx4 v[130:133], v[166:167], off offset:512
	global_load_dwordx4 v[134:137], v[166:167], off
	global_load_dwordx4 v[142:145], v[138:139], off offset:512
	s_nop 0
	global_load_dwordx4 v[138:141], v[138:139], off
	ds_read_b64_tr_b16 v[208:209], v169 offset:0
	ds_read_b64_tr_b16 v[210:211], v169 offset:0x800
	ds_read_b64_tr_b16 v[212:213], v169 offset:0x1000
	ds_read_b64_tr_b16 v[214:215], v169 offset:0x1800
	ds_read_b64_tr_b16 v[218:219], v169 offset:0x2000
	ds_read_b64_tr_b16 v[220:221], v169 offset:0x2800
	ds_read_b64_tr_b16 v[222:223], v169 offset:0x3000
	ds_read_b64_tr_b16 v[224:225], v169 offset:0x3800
	s_waitcnt lgkmcnt(0)
	s_nop 0
	v_mfma_f32_32x32x16_bf16 v[0:15], v[204:207], v[208:211], v[0:15]
	ds_read_b64_tr_b16 v[208:209], v169 offset:0x200
	ds_read_b64_tr_b16 v[210:211], v169 offset:0xa00
	v_mfma_f32_32x32x16_bf16 v[0:15], v[190:193], v[212:215], v[0:15]
	ds_read_b64_tr_b16 v[212:213], v169 offset:0x1200
	ds_read_b64_tr_b16 v[214:215], v169 offset:0x1a00
	v_mfma_f32_32x32x16_bf16 v[0:15], v[194:197], v[218:221], v[0:15]
	ds_read_b64_tr_b16 v[218:219], v169 offset:0x2200
	ds_read_b64_tr_b16 v[220:221], v169 offset:0x2a00
	v_mfma_f32_32x32x16_bf16 v[0:15], v[198:201], v[222:225], v[0:15]
	ds_read_b64_tr_b16 v[222:223], v169 offset:0x3200
	ds_read_b64_tr_b16 v[224:225], v169 offset:0x3a00
	s_waitcnt lgkmcnt(0)
	v_mfma_f32_32x32x16_bf16 v[48:63], v[204:207], v[208:211], v[48:63]
	ds_read_b64_tr_b16 v[208:209], v169 offset:0x400
	ds_read_b64_tr_b16 v[210:211], v169 offset:0xc00
	v_mfma_f32_32x32x16_bf16 v[48:63], v[190:193], v[212:215], v[48:63]
	ds_read_b64_tr_b16 v[212:213], v169 offset:0x1400
	ds_read_b64_tr_b16 v[214:215], v169 offset:0x1c00
	v_mfma_f32_32x32x16_bf16 v[48:63], v[194:197], v[218:221], v[48:63]
	ds_read_b64_tr_b16 v[218:219], v169 offset:0x2400
	ds_read_b64_tr_b16 v[220:221], v169 offset:0x2c00
	v_mfma_f32_32x32x16_bf16 v[48:63], v[198:201], v[222:225], v[48:63]
	ds_read_b64_tr_b16 v[222:223], v169 offset:0x3400
	ds_read_b64_tr_b16 v[224:225], v169 offset:0x3c00
	s_waitcnt lgkmcnt(0)
	v_mfma_f32_32x32x16_bf16 v[32:47], v[204:207], v[208:211], v[32:47]
	ds_read_b64_tr_b16 v[208:209], v169 offset:0x600
	ds_read_b64_tr_b16 v[210:211], v169 offset:0xe00
	v_mfma_f32_32x32x16_bf16 v[32:47], v[190:193], v[212:215], v[32:47]
	ds_read_b64_tr_b16 v[212:213], v169 offset:0x1600
	ds_read_b64_tr_b16 v[214:215], v169 offset:0x1e00
	v_mfma_f32_32x32x16_bf16 v[32:47], v[194:197], v[218:221], v[32:47]
	ds_read_b64_tr_b16 v[218:219], v169 offset:0x2600
	ds_read_b64_tr_b16 v[220:221], v169 offset:0x2e00
	v_mfma_f32_32x32x16_bf16 v[32:47], v[198:201], v[222:225], v[32:47]
	ds_read_b64_tr_b16 v[222:223], v169 offset:0x3600
	ds_read_b64_tr_b16 v[224:225], v169 offset:0x3e00
	s_waitcnt lgkmcnt(0)
	v_mfma_f32_32x32x16_bf16 v[16:31], v[204:207], v[208:211], v[16:31]
	v_max_f32_e32 v189, v81, v81
	s_barrier
	s_waitcnt vmcnt(0)
	s_waitcnt vmcnt(3)
	ds_write_b128 v173, v[130:133]
	s_waitcnt vmcnt(1)
	ds_write_b128 v174, v[142:145]
	ds_write_b128 v175, v[134:137] offset:32768
	s_waitcnt vmcnt(0)
	ds_write_b128 v176, v[138:141] offset:32768
	v_mfma_f32_32x32x16_bf16 v[16:31], v[190:193], v[212:215], v[16:31]
	v_max_f32_e32 v190, v80, v80
	v_max_f32_e32 v189, v190, v189
	v_max3_f32 v189, v189, v82, v83
	v_max3_f32 v189, v189, v84, v85
	v_max3_f32 v189, v189, v86, v87
	v_max3_f32 v189, v189, v88, v89
	v_max3_f32 v189, v189, v90, v91
	v_max3_f32 v189, v189, v92, v93
	v_max3_f32 v189, v189, v94, v95
	v_max3_f32 v189, v189, v64, v65
	v_max3_f32 v189, v189, v66, v67
	v_max3_f32 v189, v189, v68, v69
	v_max3_f32 v189, v189, v70, v71
	v_max3_f32 v189, v189, v72, v73
	v_max3_f32 v189, v189, v74, v75
	v_max3_f32 v189, v189, v76, v77
	v_mfma_f32_32x32x16_bf16 v[16:31], v[194:197], v[218:221], v[16:31]
	v_max3_f32 v189, v189, v78, v79
	v_mov_b32_e32 v190, v189
	s_nop 1
	v_permlane32_swap_b32_e32 v189, v190
	v_max_f32_e32 v190, v190, v190
	v_max_f32_e32 v189, v189, v189
	v_max_f32_e32 v189, v189, v190
	v_sub_f32_e32 v190, v189, v186
	v_cmp_ge_f32_e32 vcc, s73, v190
	v_max_f32_e32 v190, v186, v186
	v_max_f32_e32 v189, v190, v189
	v_mfma_f32_32x32x16_bf16 v[16:31], v[198:201], v[222:225], v[16:31]
	v_sub_f32_e32 v190, v186, v189
	v_mul_f32_e32 v190, 0x3e0293ee, v190
	v_exp_f32_e32 v190, v190
	s_cmp_eq_u64 vcc, exec
	s_cselect_b64 s[4:5], -1, 0
	v_cndmask_b32_e64 v190, v190, 1.0, s[4:5]
	v_cmp_gt_f32_e32 vcc, 1.0, v190
	s_cbranch_vccz .LBB0_850
	s_and_saveexec_b64 s[8:9], s[2:3]
	ds_write_b32 v171, v190 offset:128
	s_or_b64 exec, exec, s[8:9]
	s_waitcnt lgkmcnt(0)
	v_add_u32_e32 v142, v168, v170
	ds_read_b128 v[130:133], v142 offset:224
	ds_read_b128 v[134:137], v142 offset:192
	ds_read_b128 v[138:141], v142 offset:160
	ds_read_b128 v[142:145], v142 offset:128
	s_waitcnt lgkmcnt(3)
	v_pk_mul_f32 v[12:13], v[12:13], v[130:131]
	s_waitcnt lgkmcnt(2)
	v_pk_mul_f32 v[8:9], v[8:9], v[134:135]
	s_waitcnt lgkmcnt(1)
	v_pk_mul_f32 v[4:5], v[4:5], v[138:139]
	v_pk_mul_f32 v[14:15], v[14:15], v[132:133]
	v_pk_mul_f32 v[10:11], v[10:11], v[136:137]
	v_pk_mul_f32 v[6:7], v[6:7], v[140:141]
	s_waitcnt lgkmcnt(0)
	v_pk_mul_f32 v[2:3], v[2:3], v[144:145]
	v_pk_mul_f32 v[0:1], v[0:1], v[142:143]
	v_pk_mul_f32 v[60:61], v[60:61], v[130:131]
	v_pk_mul_f32 v[56:57], v[56:57], v[134:135]
	v_pk_mul_f32 v[52:53], v[52:53], v[138:139]
	v_pk_mul_f32 v[62:63], v[62:63], v[132:133]
	v_pk_mul_f32 v[58:59], v[58:59], v[136:137]
	v_pk_mul_f32 v[54:55], v[54:55], v[140:141]
	v_pk_mul_f32 v[50:51], v[50:51], v[144:145]
	v_pk_mul_f32 v[48:49], v[48:49], v[142:143]
	v_pk_mul_f32 v[44:45], v[44:45], v[130:131]
	v_pk_mul_f32 v[40:41], v[40:41], v[134:135]
	v_pk_mul_f32 v[36:37], v[36:37], v[138:139]
	v_pk_mul_f32 v[46:47], v[46:47], v[132:133]
	v_pk_mul_f32 v[42:43], v[42:43], v[136:137]
	v_pk_mul_f32 v[38:39], v[38:39], v[140:141]
	v_pk_mul_f32 v[34:35], v[34:35], v[144:145]
	v_pk_mul_f32 v[32:33], v[32:33], v[142:143]
	v_pk_mul_f32 v[28:29], v[28:29], v[130:131]
	v_pk_mul_f32 v[24:25], v[24:25], v[134:135]
	v_pk_mul_f32 v[20:21], v[20:21], v[138:139]
	v_pk_mul_f32 v[30:31], v[30:31], v[132:133]
	v_pk_mul_f32 v[26:27], v[26:27], v[136:137]
	v_pk_mul_f32 v[22:23], v[22:23], v[140:141]
	v_pk_mul_f32 v[18:19], v[18:19], v[144:145]
	v_pk_mul_f32 v[16:17], v[16:17], v[142:143]
.LBB0_850:
	v_cndmask_b32_e64 v186, v189, v186, s[4:5]
	v_mul_f32_e32 v189, 0xbe0293ee, v186
	v_fmamk_f32 v80, v80, 0x3e0293ee, v189
	v_fmamk_f32 v81, v81, 0x3e0293ee, v189
	v_fmamk_f32 v82, v82, 0x3e0293ee, v189
	v_fmamk_f32 v83, v83, 0x3e0293ee, v189
	v_fmamk_f32 v84, v84, 0x3e0293ee, v189
	v_fmamk_f32 v85, v85, 0x3e0293ee, v189
	v_fmamk_f32 v86, v86, 0x3e0293ee, v189
	v_fmamk_f32 v87, v87, 0x3e0293ee, v189
	v_fmamk_f32 v88, v88, 0x3e0293ee, v189
	v_fmamk_f32 v89, v89, 0x3e0293ee, v189
	v_fmamk_f32 v90, v90, 0x3e0293ee, v189
	v_fmamk_f32 v91, v91, 0x3e0293ee, v189
	v_fmamk_f32 v92, v92, 0x3e0293ee, v189
	v_fmamk_f32 v93, v93, 0x3e0293ee, v189
	v_fmamk_f32 v94, v94, 0x3e0293ee, v189
	v_fmamk_f32 v95, v95, 0x3e0293ee, v189
	v_fmamk_f32 v199, v64, 0x3e0293ee, v189
	v_fmamk_f32 v200, v65, 0x3e0293ee, v189
	v_fmamk_f32 v201, v66, 0x3e0293ee, v189
	v_fmamk_f32 v202, v67, 0x3e0293ee, v189
	v_fmamk_f32 v203, v68, 0x3e0293ee, v189
	v_fmamk_f32 v192, v69, 0x3e0293ee, v189
	v_fmamk_f32 v193, v70, 0x3e0293ee, v189
	v_fmamk_f32 v194, v71, 0x3e0293ee, v189
	v_fmamk_f32 v195, v72, 0x3e0293ee, v189
	v_fmamk_f32 v196, v73, 0x3e0293ee, v189
	v_fmamk_f32 v197, v74, 0x3e0293ee, v189
	v_fmamk_f32 v198, v75, 0x3e0293ee, v189
	v_fmamk_f32 v191, v76, 0x3e0293ee, v189
	v_fmamk_f32 v221, v77, 0x3e0293ee, v189
	v_fmamk_f32 v222, v78, 0x3e0293ee, v189
	v_fmac_f32_e32 v189, 0x3e0293ee, v79
	v_exp_f32_e32 v139, v80
	v_exp_f32_e32 v141, v81
	v_exp_f32_e32 v142, v82
	v_exp_f32_e32 v143, v83
	v_exp_f32_e32 v144, v84
	v_exp_f32_e32 v145, v85
	v_exp_f32_e32 v138, v86
	v_exp_f32_e32 v140, v87
	v_exp_f32_e32 v133, v88
	v_exp_f32_e32 v135, v89
	v_exp_f32_e32 v136, v90
	v_exp_f32_e32 v137, v91
	v_exp_f32_e32 v130, v92
	v_exp_f32_e32 v131, v93
	v_exp_f32_e32 v132, v94
	v_exp_f32_e32 v134, v95
	s_waitcnt lgkmcnt(0)
	s_barrier
	ds_read_b128 v[64:67], v177 offset:32768
	ds_read_b128 v[68:71], v177 offset:40960
	ds_read_b128 v[204:207], v178 offset:32768
	ds_read_b128 v[208:211], v178 offset:40960
	ds_read_b128 v[230:233], v179 offset:32768
	ds_read_b128 v[234:237], v179 offset:40960
	v_exp_f32_e32 v215, v191
	v_add_f32_e32 v191, 0, v139
	s_waitcnt lgkmcnt(5)
	v_mfma_f32_32x32x16_bf16 v[80:95], v[64:67], v[126:129], 0
	v_add_f32_e32 v191, v141, v191
	v_add_f32_e32 v191, v142, v191
	v_add_f32_e32 v191, v143, v191
	v_add_f32_e32 v191, v144, v191
	v_add_f32_e32 v191, v145, v191
	v_add_f32_e32 v191, v138, v191
	v_add_f32_e32 v191, v140, v191
	s_waitcnt lgkmcnt(4)
	v_mfma_f32_32x32x16_bf16 v[64:79], v[68:71], v[126:129], 0
	v_add_f32_e32 v191, v133, v191
	v_add_f32_e32 v191, v135, v191
	v_add_f32_e32 v191, v136, v191
	v_add_f32_e32 v191, v137, v191
	v_add_f32_e32 v191, v130, v191
	v_add_f32_e32 v191, v131, v191
	v_add_f32_e32 v191, v132, v191
	s_waitcnt lgkmcnt(3)
	v_mfma_f32_32x32x16_bf16 v[80:95], v[204:207], v[122:125], v[80:95]
	v_add_f32_e32 v191, v134, v191
	v_exp_f32_e32 v193, v193
	v_exp_f32_e32 v212, v196
	v_exp_f32_e32 v213, v197
	v_exp_f32_e32 v214, v198
	v_exp_f32_e32 v218, v221
	v_exp_f32_e32 v219, v222
	s_waitcnt lgkmcnt(2)
	v_mfma_f32_32x32x16_bf16 v[64:79], v[208:211], v[122:125], v[64:79]
	ds_read_b128 v[204:207], v180 offset:32768
	ds_read_b128 v[208:211], v180 offset:40960
	v_exp_f32_e32 v189, v189
	v_cvt_pk_bf16_f32 v196, v144, v145
	v_cvt_pk_bf16_f32 v197, v138, v140
	v_cvt_pk_bf16_f32 v198, v133, v135
	s_waitcnt lgkmcnt(3)
	v_mfma_f32_32x32x16_bf16 v[80:95], v[230:233], v[118:121], v[80:95]
	s_waitcnt lgkmcnt(2)
	v_mfma_f32_32x32x16_bf16 v[64:79], v[234:237], v[118:121], v[64:79]
	ds_read_b128 v[230:233], v181 offset:32768
	ds_read_b128 v[234:237], v181 offset:40960
	s_waitcnt lgkmcnt(3)
	v_mfma_f32_32x32x16_bf16 v[80:95], v[204:207], v[114:117], v[80:95]
	s_waitcnt lgkmcnt(2)
	v_mfma_f32_32x32x16_bf16 v[64:79], v[208:211], v[114:117], v[64:79]
	ds_read_b128 v[204:207], v182 offset:32768
	ds_read_b128 v[208:211], v182 offset:40960
	s_waitcnt lgkmcnt(3)
	v_mfma_f32_32x32x16_bf16 v[80:95], v[230:233], v[110:113], v[80:95]
	s_waitcnt lgkmcnt(2)
	v_mfma_f32_32x32x16_bf16 v[64:79], v[234:237], v[110:113], v[64:79]
	ds_read_b128 v[230:233], v183 offset:32768
	ds_read_b128 v[234:237], v183 offset:40960
	s_waitcnt lgkmcnt(3)
	v_mfma_f32_32x32x16_bf16 v[80:95], v[204:207], v[106:109], v[80:95]
	s_waitcnt lgkmcnt(2)
	v_mfma_f32_32x32x16_bf16 v[64:79], v[208:211], v[106:109], v[64:79]
	ds_read_b128 v[204:207], v184 offset:32768
	ds_read_b128 v[208:211], v184 offset:40960
	s_waitcnt lgkmcnt(3)
	v_mfma_f32_32x32x16_bf16 v[80:95], v[230:233], v[102:105], v[80:95]
	s_waitcnt lgkmcnt(2)
	v_mfma_f32_32x32x16_bf16 v[64:79], v[234:237], v[102:105], v[64:79]
	s_waitcnt lgkmcnt(1)
	v_mfma_f32_32x32x16_bf16 v[80:95], v[204:207], v[98:101], v[80:95]
	v_exp_f32_e32 v204, v199
	v_exp_f32_e32 v205, v200
	v_exp_f32_e32 v206, v201
	v_exp_f32_e32 v207, v202
	v_add_f32_e32 v191, v204, v191
	v_add_f32_e32 v191, v205, v191
	v_add_f32_e32 v191, v206, v191
	s_waitcnt lgkmcnt(0)
	v_mfma_f32_32x32x16_bf16 v[64:79], v[208:211], v[98:101], v[64:79]
	v_exp_f32_e32 v208, v203
	v_exp_f32_e32 v209, v192
	v_exp_f32_e32 v210, v194
	v_add_f32_e32 v191, v207, v191
	v_exp_f32_e32 v211, v195
	v_add_f32_e32 v191, v208, v191
	v_add_f32_e32 v191, v209, v191
	v_add_f32_e32 v191, v193, v191
	v_add_f32_e32 v191, v210, v191
	v_add_f32_e32 v191, v211, v191
	v_add_f32_e32 v191, v212, v191
	v_add_f32_e32 v191, v213, v191
	v_add_f32_e32 v191, v214, v191
	v_add_f32_e32 v191, v215, v191
	v_add_f32_e32 v191, v218, v191
	v_add_f32_e32 v191, v219, v191
	v_add_f32_e32 v191, v189, v191
	v_mov_b32_e32 v192, v191
	s_nop 1
	v_permlane32_swap_b32_e32 v191, v192
	v_cvt_pk_bf16_f32 v194, v139, v141
	v_cvt_pk_bf16_f32 v195, v142, v143
	v_cvt_pk_bf16_f32 v199, v136, v137
	v_cvt_pk_bf16_f32 v200, v130, v131
	v_cvt_pk_bf16_f32 v201, v132, v134
	v_cvt_pk_bf16_f32 v202, v204, v205
	v_cvt_pk_bf16_f32 v203, v206, v207
	v_cvt_pk_bf16_f32 v204, v208, v209
	v_cvt_pk_bf16_f32 v205, v193, v210
	v_cvt_pk_bf16_f32 v206, v211, v212
	v_cvt_pk_bf16_f32 v207, v213, v214
	v_cvt_pk_bf16_f32 v208, v215, v218
	v_cvt_pk_bf16_f32 v209, v219, v189
	v_permlane32_swap_b32_e32 v194, v196
	v_permlane32_swap_b32_e32 v195, v197
	v_permlane32_swap_b32_e32 v198, v200
	v_permlane32_swap_b32_e32 v199, v201
	v_permlane32_swap_b32_e32 v202, v204
	v_permlane32_swap_b32_e32 v203, v205
	v_permlane32_swap_b32_e32 v206, v208
	v_permlane32_swap_b32_e32 v207, v209
	v_add_co_u32_e32 v134, vcc, s49, v166
	s_nop 1
	v_addc_co_u32_e32 v135, vcc, 0, v167, vcc
	v_add_co_u32_e32 v138, vcc, s64, v166
	s_nop 1
	v_addc_co_u32_e32 v139, vcc, 0, v167, vcc
	global_load_dwordx4 v[130:133], v[134:135], off offset:512
	s_nop 0
	global_load_dwordx4 v[134:137], v[134:135], off
	s_nop 0
	global_load_dwordx4 v[142:145], v[138:139], off offset:512
	s_nop 0
	global_load_dwordx4 v[138:141], v[138:139], off
	ds_read_b64_tr_b16 v[210:211], v172 offset:0
	ds_read_b64_tr_b16 v[212:213], v172 offset:0x800
	ds_read_b64_tr_b16 v[218:219], v172 offset:0x1000
	ds_read_b64_tr_b16 v[220:221], v172 offset:0x1800
	ds_read_b64_tr_b16 v[222:223], v172 offset:0x2000
	ds_read_b64_tr_b16 v[224:225], v172 offset:0x2800
	ds_read_b64_tr_b16 v[226:227], v172 offset:0x3000
	ds_read_b64_tr_b16 v[228:229], v172 offset:0x3800
	s_waitcnt lgkmcnt(0)
	s_nop 0
	v_mfma_f32_32x32x16_bf16 v[0:15], v[194:197], v[210:213], v[0:15]
	ds_read_b64_tr_b16 v[210:211], v172 offset:0x200
	ds_read_b64_tr_b16 v[212:213], v172 offset:0xa00
	v_mfma_f32_32x32x16_bf16 v[0:15], v[198:201], v[218:221], v[0:15]
	ds_read_b64_tr_b16 v[218:219], v172 offset:0x1200
	ds_read_b64_tr_b16 v[220:221], v172 offset:0x1a00
	v_mfma_f32_32x32x16_bf16 v[0:15], v[202:205], v[222:225], v[0:15]
	ds_read_b64_tr_b16 v[222:223], v172 offset:0x2200
	ds_read_b64_tr_b16 v[224:225], v172 offset:0x2a00
	v_mfma_f32_32x32x16_bf16 v[0:15], v[206:209], v[226:229], v[0:15]
	ds_read_b64_tr_b16 v[226:227], v172 offset:0x3200
	ds_read_b64_tr_b16 v[228:229], v172 offset:0x3a00
	s_waitcnt lgkmcnt(0)
	v_mfma_f32_32x32x16_bf16 v[48:63], v[194:197], v[210:213], v[48:63]
	ds_read_b64_tr_b16 v[210:211], v172 offset:0x400
	ds_read_b64_tr_b16 v[212:213], v172 offset:0xc00
	v_mfma_f32_32x32x16_bf16 v[48:63], v[198:201], v[218:221], v[48:63]
	ds_read_b64_tr_b16 v[218:219], v172 offset:0x1400
	ds_read_b64_tr_b16 v[220:221], v172 offset:0x1c00
	v_mfma_f32_32x32x16_bf16 v[48:63], v[202:205], v[222:225], v[48:63]
	ds_read_b64_tr_b16 v[222:223], v172 offset:0x2400
	ds_read_b64_tr_b16 v[224:225], v172 offset:0x2c00
	v_mfma_f32_32x32x16_bf16 v[48:63], v[206:209], v[226:229], v[48:63]
	ds_read_b64_tr_b16 v[226:227], v172 offset:0x3400
	ds_read_b64_tr_b16 v[228:229], v172 offset:0x3c00
	s_waitcnt lgkmcnt(0)
	v_mfma_f32_32x32x16_bf16 v[32:47], v[194:197], v[210:213], v[32:47]
	ds_read_b64_tr_b16 v[210:211], v172 offset:0x600
	ds_read_b64_tr_b16 v[212:213], v172 offset:0xe00
	v_mfma_f32_32x32x16_bf16 v[32:47], v[198:201], v[218:221], v[32:47]
	ds_read_b64_tr_b16 v[218:219], v172 offset:0x1600
	ds_read_b64_tr_b16 v[220:221], v172 offset:0x1e00
	v_mfma_f32_32x32x16_bf16 v[32:47], v[202:205], v[222:225], v[32:47]
	ds_read_b64_tr_b16 v[222:223], v172 offset:0x2600
	ds_read_b64_tr_b16 v[224:225], v172 offset:0x2e00
	v_mfma_f32_32x32x16_bf16 v[32:47], v[206:209], v[226:229], v[32:47]
	ds_read_b64_tr_b16 v[226:227], v172 offset:0x3600
	ds_read_b64_tr_b16 v[228:229], v172 offset:0x3e00
	s_waitcnt lgkmcnt(0)
	v_mfma_f32_32x32x16_bf16 v[16:31], v[194:197], v[210:213], v[16:31]
	v_max_f32_e32 v189, v81, v81
	v_max_f32_e32 v193, v80, v80
	v_max_f32_e32 v189, v193, v189
	v_max3_f32 v189, v189, v82, v83
	v_max3_f32 v189, v189, v84, v85
	v_max3_f32 v189, v189, v86, v87
	v_max3_f32 v189, v189, v88, v89
	v_max3_f32 v189, v189, v90, v91
	v_max3_f32 v189, v189, v92, v93
	v_mfma_f32_32x32x16_bf16 v[16:31], v[198:201], v[218:221], v[16:31]
	v_max3_f32 v189, v189, v94, v95
	v_max3_f32 v189, v189, v64, v65
	v_max3_f32 v189, v189, v66, v67
	v_max3_f32 v189, v189, v68, v69
	v_max3_f32 v189, v189, v70, v71
	v_max3_f32 v189, v189, v72, v73
	v_max3_f32 v189, v189, v74, v75
	v_max3_f32 v189, v189, v76, v77
	v_mfma_f32_32x32x16_bf16 v[16:31], v[202:205], v[222:225], v[16:31]
	v_max3_f32 v189, v189, v78, v79
	v_mov_b32_e32 v193, v189
	s_nop 1
	v_permlane32_swap_b32_e32 v189, v193
	v_max_f32_e32 v193, v193, v193
	v_max_f32_e32 v189, v189, v189
	v_max_f32_e32 v189, v189, v193
	v_sub_f32_e32 v193, v189, v186
	v_cmp_ge_f32_e32 vcc, s73, v193
	v_max_f32_e32 v193, v186, v186
	v_max_f32_e32 v193, v193, v189
	v_mfma_f32_32x32x16_bf16 v[16:31], v[206:209], v[226:229], v[16:31]
	v_sub_f32_e32 v189, v186, v193
	v_mul_f32_e32 v189, 0x3e0293ee, v189
	v_exp_f32_e32 v189, v189
	s_cmp_eq_u64 vcc, exec
	s_cselect_b64 s[4:5], -1, 0
	s_barrier
	s_waitcnt vmcnt(0)
	v_cndmask_b32_e64 v189, v189, 1.0, s[4:5]
	v_cmp_gt_f32_e32 vcc, 1.0, v189
	s_waitcnt vmcnt(3)
	ds_write_b128 v173, v[130:133] offset:16384
	s_waitcnt vmcnt(1)
	ds_write_b128 v174, v[142:145] offset:16384
	ds_write_b128 v175, v[134:137] offset:49152
	s_waitcnt vmcnt(0)
	ds_write_b128 v176, v[138:141] offset:49152
	s_cbranch_vccz .LBB0_854
	s_and_saveexec_b64 s[8:9], s[2:3]
	ds_write_b32 v171, v189 offset:128
	s_or_b64 exec, exec, s[8:9]
	s_waitcnt lgkmcnt(0)
	v_add_u32_e32 v142, v168, v170
	ds_read_b128 v[130:133], v142 offset:224
	ds_read_b128 v[134:137], v142 offset:192
	ds_read_b128 v[138:141], v142 offset:160
	ds_read_b128 v[142:145], v142 offset:128
	s_waitcnt lgkmcnt(3)
	v_pk_mul_f32 v[12:13], v[12:13], v[130:131]
	s_waitcnt lgkmcnt(2)
	v_pk_mul_f32 v[8:9], v[8:9], v[134:135]
	s_waitcnt lgkmcnt(1)
	v_pk_mul_f32 v[4:5], v[4:5], v[138:139]
	v_pk_mul_f32 v[14:15], v[14:15], v[132:133]
	v_pk_mul_f32 v[10:11], v[10:11], v[136:137]
	v_pk_mul_f32 v[6:7], v[6:7], v[140:141]
	s_waitcnt lgkmcnt(0)
	v_pk_mul_f32 v[2:3], v[2:3], v[144:145]
	v_pk_mul_f32 v[0:1], v[0:1], v[142:143]
	v_pk_mul_f32 v[60:61], v[60:61], v[130:131]
	v_pk_mul_f32 v[56:57], v[56:57], v[134:135]
	v_pk_mul_f32 v[52:53], v[52:53], v[138:139]
	v_pk_mul_f32 v[62:63], v[62:63], v[132:133]
	v_pk_mul_f32 v[58:59], v[58:59], v[136:137]
	v_pk_mul_f32 v[54:55], v[54:55], v[140:141]
	v_pk_mul_f32 v[50:51], v[50:51], v[144:145]
	v_pk_mul_f32 v[48:49], v[48:49], v[142:143]
	v_pk_mul_f32 v[44:45], v[44:45], v[130:131]
	v_pk_mul_f32 v[40:41], v[40:41], v[134:135]
	v_pk_mul_f32 v[36:37], v[36:37], v[138:139]
	v_pk_mul_f32 v[46:47], v[46:47], v[132:133]
	v_pk_mul_f32 v[42:43], v[42:43], v[136:137]
	v_pk_mul_f32 v[38:39], v[38:39], v[140:141]
	v_pk_mul_f32 v[34:35], v[34:35], v[144:145]
	v_pk_mul_f32 v[32:33], v[32:33], v[142:143]
	v_pk_mul_f32 v[28:29], v[28:29], v[130:131]
	v_pk_mul_f32 v[24:25], v[24:25], v[134:135]
	v_pk_mul_f32 v[20:21], v[20:21], v[138:139]
	v_pk_mul_f32 v[30:31], v[30:31], v[132:133]
	v_pk_mul_f32 v[26:27], v[26:27], v[136:137]
	v_pk_mul_f32 v[22:23], v[22:23], v[140:141]
	v_pk_mul_f32 v[18:19], v[18:19], v[144:145]
	v_pk_mul_f32 v[16:17], v[16:17], v[142:143]
